# stack17
# speedup vs baseline: 1.0035x; 1.0029x over previous
_Z7k_spmm1PKiS0_PKfPK15HIP_vector_typeIjLj2EES0_S2_S2_Pfff:
	s_load_dwordx8 s[4:11], s[0:1], 0x18
	s_load_dwordx2 s[20:21], s[0:1], 0x0
	s_load_dwordx4 s[24:27], s[0:1], 0x38
	v_and_b32_e32 v10, 63, v0
	s_lshl_b32 s2, s2, 4
	v_lshrrev_b32_e32 v0, 5, v0
	v_and_or_b32 v0, v0, 14, s2
	s_nop 0
	v_readfirstlane_b32 s2, v0
	s_ashr_i32 s3, s2, 31
	s_lshl_b64 s[12:13], s[2:3], 8
	s_waitcnt lgkmcnt(0)
	s_add_u32 s4, s4, s12
	s_addc_u32 s5, s5, s13
	s_lshl_b64 s[12:13], s[2:3], 2
	s_add_u32 s22, s20, s12
	s_addc_u32 s23, s21, s13
	s_load_dwordx2 s[28:29], s[22:23], 0x0
	s_load_dword s30, s[22:23], 0x8
	s_add_u32 s6, s6, s12
	v_lshlrev_b32_e32 v0, 3, v10
	s_addc_u32 s7, s7, s13
	s_lshl_b64 s[2:3], s[2:3], 6
	global_load_dwordx2 v[6:7], v0, s[4:5]
	v_or_b32_e32 v0, s2, v10
	v_mov_b32_e32 v1, s3
	v_lshlrev_b64 v[0:1], 2, v[0:1]
	v_lshl_add_u64 v[8:9], s[10:11], 0, v[0:1]
	v_lshl_add_u64 v[0:1], s[8:9], 0, v[0:1]
	global_load_dword v4, v[8:9], off
	global_load_dword v2, v[8:9], off offset:256
	global_load_dword v5, v[0:1], off
	global_load_dword v3, v[0:1], off offset:256
	s_load_dwordx2 s[4:5], s[6:7], 0x0
	v_lshlrev_b32_e32 v0, 2, v10
	s_waitcnt lgkmcnt(0)
	s_cmp_gt_i32 s4, 16
	s_cbranch_scc0 .LBB1_3
	s_cmp_gt_u32 s4, 24
	s_cbranch_scc0 .LBB1_4
	s_mov_b32 s7, 0
	s_waitcnt vmcnt(4)
	v_readlane_b32 s6, v6, 0
	s_lshl_b64 s[8:9], s[6:7], 8
	s_add_u32 s8, s10, s8
	s_addc_u32 s9, s11, s9
	v_readlane_b32 s6, v6, 1
	global_load_dword v1, v0, s[8:9]
	s_lshl_b64 s[8:9], s[6:7], 8
	s_add_u32 s8, s10, s8
	s_addc_u32 s9, s11, s9
	v_readlane_b32 s6, v6, 2
	global_load_dword v9, v0, s[8:9]
	s_lshl_b64 s[8:9], s[6:7], 8
	s_add_u32 s8, s10, s8
	s_addc_u32 s9, s11, s9
	v_readlane_b32 s6, v6, 3
	global_load_dword v10, v0, s[8:9]
	s_lshl_b64 s[8:9], s[6:7], 8
	s_add_u32 s8, s10, s8
	s_addc_u32 s9, s11, s9
	v_readlane_b32 s6, v6, 4
	global_load_dword v11, v0, s[8:9]
	s_lshl_b64 s[8:9], s[6:7], 8
	s_add_u32 s8, s10, s8
	s_addc_u32 s9, s11, s9
	v_readlane_b32 s6, v6, 5
	global_load_dword v12, v0, s[8:9]
	s_lshl_b64 s[8:9], s[6:7], 8
	s_add_u32 s8, s10, s8
	s_addc_u32 s9, s11, s9
	v_readlane_b32 s6, v6, 6
	global_load_dword v13, v0, s[8:9]
	s_lshl_b64 s[8:9], s[6:7], 8
	s_add_u32 s8, s10, s8
	s_addc_u32 s9, s11, s9
	v_readlane_b32 s6, v6, 7
	global_load_dword v14, v0, s[8:9]
	s_lshl_b64 s[8:9], s[6:7], 8
	s_add_u32 s8, s10, s8
	s_addc_u32 s9, s11, s9
	v_readlane_b32 s6, v6, 8
	global_load_dword v15, v0, s[8:9]
	s_lshl_b64 s[8:9], s[6:7], 8
	s_add_u32 s8, s10, s8
	s_addc_u32 s9, s11, s9
	v_readlane_b32 s6, v6, 9
	global_load_dword v16, v0, s[8:9]
	s_lshl_b64 s[8:9], s[6:7], 8
	s_add_u32 s8, s10, s8
	s_addc_u32 s9, s11, s9
	v_readlane_b32 s6, v6, 10
	global_load_dword v17, v0, s[8:9]
	s_lshl_b64 s[8:9], s[6:7], 8
	s_add_u32 s8, s10, s8
	s_addc_u32 s9, s11, s9
	v_readlane_b32 s6, v6, 11
	global_load_dword v18, v0, s[8:9]
	s_lshl_b64 s[8:9], s[6:7], 8
	s_add_u32 s8, s10, s8
	s_addc_u32 s9, s11, s9
	v_readlane_b32 s6, v6, 12
	global_load_dword v19, v0, s[8:9]
	s_lshl_b64 s[8:9], s[6:7], 8
	s_add_u32 s8, s10, s8
	s_addc_u32 s9, s11, s9
	v_readlane_b32 s6, v6, 13
	global_load_dword v20, v0, s[8:9]
	s_lshl_b64 s[8:9], s[6:7], 8
	s_add_u32 s8, s10, s8
	s_addc_u32 s9, s11, s9
	v_readlane_b32 s6, v6, 14
	global_load_dword v21, v0, s[8:9]
	s_lshl_b64 s[8:9], s[6:7], 8
	s_add_u32 s8, s10, s8
	s_addc_u32 s9, s11, s9
	v_readlane_b32 s6, v6, 15
	global_load_dword v22, v0, s[8:9]
	s_lshl_b64 s[8:9], s[6:7], 8
	s_add_u32 s8, s10, s8
	s_addc_u32 s9, s11, s9
	v_readlane_b32 s6, v6, 16
	global_load_dword v23, v0, s[8:9]
	s_lshl_b64 s[8:9], s[6:7], 8
	s_add_u32 s8, s10, s8
	s_addc_u32 s9, s11, s9
	v_readlane_b32 s6, v6, 17
	global_load_dword v24, v0, s[8:9]
	s_lshl_b64 s[8:9], s[6:7], 8
	s_add_u32 s8, s10, s8
	s_addc_u32 s9, s11, s9
	v_readlane_b32 s6, v6, 18
	global_load_dword v25, v0, s[8:9]
	s_lshl_b64 s[8:9], s[6:7], 8
	s_add_u32 s8, s10, s8
	s_addc_u32 s9, s11, s9
	v_readlane_b32 s6, v6, 19
	global_load_dword v26, v0, s[8:9]
	s_lshl_b64 s[8:9], s[6:7], 8
	s_add_u32 s8, s10, s8
	s_addc_u32 s9, s11, s9
	v_readlane_b32 s6, v6, 20
	global_load_dword v27, v0, s[8:9]
	s_lshl_b64 s[8:9], s[6:7], 8
	s_add_u32 s8, s10, s8
	s_addc_u32 s9, s11, s9
	v_readlane_b32 s6, v6, 21
	global_load_dword v28, v0, s[8:9]
	s_lshl_b64 s[8:9], s[6:7], 8
	s_add_u32 s8, s10, s8
	s_addc_u32 s9, s11, s9
	v_readlane_b32 s6, v6, 22
	global_load_dword v29, v0, s[8:9]
	s_lshl_b64 s[8:9], s[6:7], 8
	s_add_u32 s8, s10, s8
	s_addc_u32 s9, s11, s9
	v_readlane_b32 s6, v6, 23
	global_load_dword v30, v0, s[8:9]
	s_lshl_b64 s[8:9], s[6:7], 8
	s_add_u32 s8, s10, s8
	s_addc_u32 s9, s11, s9
	v_readlane_b32 s6, v6, 24
	global_load_dword v31, v0, s[8:9]
	s_lshl_b64 s[8:9], s[6:7], 8
	s_add_u32 s8, s10, s8
	s_addc_u32 s9, s11, s9
	v_readlane_b32 s6, v6, 25
	global_load_dword v32, v0, s[8:9]
	s_lshl_b64 s[8:9], s[6:7], 8
	s_add_u32 s8, s10, s8
	s_addc_u32 s9, s11, s9
	v_readlane_b32 s6, v6, 26
	global_load_dword v33, v0, s[8:9]
	s_lshl_b64 s[8:9], s[6:7], 8
	s_add_u32 s8, s10, s8
	s_addc_u32 s9, s11, s9
	v_readlane_b32 s6, v6, 27
	global_load_dword v34, v0, s[8:9]
	s_lshl_b64 s[8:9], s[6:7], 8
	s_add_u32 s8, s10, s8
	s_addc_u32 s9, s11, s9
	v_readlane_b32 s6, v6, 28
	global_load_dword v35, v0, s[8:9]
	s_lshl_b64 s[8:9], s[6:7], 8
	s_add_u32 s8, s10, s8
	s_addc_u32 s9, s11, s9
	v_readlane_b32 s6, v6, 29
	global_load_dword v36, v0, s[8:9]
	s_lshl_b64 s[8:9], s[6:7], 8
	s_add_u32 s8, s10, s8
	s_addc_u32 s9, s11, s9
	v_readlane_b32 s6, v6, 30
	global_load_dword v37, v0, s[8:9]
	s_lshl_b64 s[8:9], s[6:7], 8
	s_add_u32 s8, s10, s8
	v_readlane_b32 s6, v6, 31
	s_addc_u32 s9, s11, s9
	s_lshl_b64 s[6:7], s[6:7], 8
	s_add_u32 s6, s10, s6
	v_readlane_b32 s4, v7, 0
	global_load_dword v38, v0, s[8:9]
	s_addc_u32 s7, s11, s7
	global_load_dword v39, v0, s[6:7]
	s_waitcnt vmcnt(0)
	s_nop 0
	v_fma_f32 v8, s4, v1, 0
	v_readlane_b32 s4, v7, 1
	s_nop 1
	v_fmac_f32_e32 v8, s4, v9
	v_readlane_b32 s4, v7, 2
	s_nop 1
	v_fmac_f32_e32 v8, s4, v10
	v_readlane_b32 s4, v7, 3
	s_nop 1
	v_fmac_f32_e32 v8, s4, v11
	v_readlane_b32 s4, v7, 4
	s_nop 1
	v_fmac_f32_e32 v8, s4, v12
	v_readlane_b32 s4, v7, 5
	s_nop 1
	v_fmac_f32_e32 v8, s4, v13
	v_readlane_b32 s4, v7, 6
	s_nop 1
	v_fmac_f32_e32 v8, s4, v14
	v_readlane_b32 s4, v7, 7
	s_nop 1
	v_fmac_f32_e32 v8, s4, v15
	v_readlane_b32 s4, v7, 8
	s_nop 1
	v_fmac_f32_e32 v8, s4, v16
	v_readlane_b32 s4, v7, 9
	s_nop 1
	v_fmac_f32_e32 v8, s4, v17
	v_readlane_b32 s4, v7, 10
	s_nop 1
	v_fmac_f32_e32 v8, s4, v18
	v_readlane_b32 s4, v7, 11
	s_nop 1
	v_fmac_f32_e32 v8, s4, v19
	v_readlane_b32 s4, v7, 12
	s_nop 1
	v_fmac_f32_e32 v8, s4, v20
	v_readlane_b32 s4, v7, 13
	s_nop 1
	v_fmac_f32_e32 v8, s4, v21
	v_readlane_b32 s4, v7, 14
	s_nop 1
	v_fmac_f32_e32 v8, s4, v22
	v_readlane_b32 s4, v7, 15
	s_nop 1
	v_fmac_f32_e32 v8, s4, v23
	v_readlane_b32 s4, v7, 16
	s_nop 1
	v_fmac_f32_e32 v8, s4, v24
	v_readlane_b32 s4, v7, 17
	s_nop 1
	v_fmac_f32_e32 v8, s4, v25
	v_readlane_b32 s4, v7, 18
	s_nop 1
	v_fmac_f32_e32 v8, s4, v26
	v_readlane_b32 s4, v7, 19
	s_nop 1
	v_fmac_f32_e32 v8, s4, v27
	v_readlane_b32 s4, v7, 20
	s_nop 1
	v_fmac_f32_e32 v8, s4, v28
	v_readlane_b32 s4, v7, 21
	s_nop 1
	v_fmac_f32_e32 v8, s4, v29
	v_readlane_b32 s4, v7, 22
	s_nop 1
	v_fmac_f32_e32 v8, s4, v30
	v_readlane_b32 s4, v7, 23
	s_nop 1
	v_fmac_f32_e32 v8, s4, v31
	v_readlane_b32 s4, v7, 24
	s_nop 1
	v_fmac_f32_e32 v8, s4, v32
	v_readlane_b32 s4, v7, 25
	s_nop 1
	v_fmac_f32_e32 v8, s4, v33
	v_readlane_b32 s4, v7, 26
	s_nop 1
	v_fmac_f32_e32 v8, s4, v34
	v_readlane_b32 s4, v7, 27
	s_nop 1
	v_fmac_f32_e32 v8, s4, v35
	v_readlane_b32 s4, v7, 28
	s_nop 1
	v_fmac_f32_e32 v8, s4, v36
	v_readlane_b32 s4, v7, 29
	s_nop 1
	v_fmac_f32_e32 v8, s4, v37
	v_readlane_b32 s4, v7, 30
	s_nop 1
	v_fmac_f32_e32 v8, s4, v38
	v_readlane_b32 s4, v7, 31
	s_nop 1
	v_fmac_f32_e32 v8, s4, v39
	s_cbranch_execz .LBB1_5
	s_branch .LBB1_6

.LBB1_16:
	s_waitcnt lgkmcnt(0)
	s_add_u32 s14, s8, s12
	s_addc_u32 s15, s9, s13
	s_mov_b64 s[12:13], s[28:29]
	s_mov_b64 s[8:9], s[24:25]
	s_mov_b32 s16, s30
	v_mov_b32_e32 v1, 0
	s_waitcnt vmcnt(4)
	v_lshl_add_u64 v[6:7], s[10:11], 0, v[0:1]
	s_waitcnt lgkmcnt(0)
	s_add_i32 s17, s12, 32
	s_cmp_ge_i32 s17, s13
	s_cbranch_scc1 .LBB1_19
	s_ashr_i32 s11, s12, 31
	s_mov_b32 s10, s12
	s_lshl_b64 s[10:11], s[10:11], 2
	s_add_u32 s12, s10, 0x80
	s_addc_u32 s15, s11, 0
	s_add_u32 s10, s6, s12
	s_addc_u32 s11, s7, s15
	s_add_u32 s14, s4, s12
	s_addc_u32 s15, s5, s15

.LBB1_22:
	s_mov_b64 s[0:1], s[26:27]
	s_waitcnt vmcnt(3)
	v_sub_f32_e32 v4, v8, v4
	s_waitcnt vmcnt(2)
	v_sub_f32_e32 v2, v9, v2
	s_waitcnt vmcnt(1) lgkmcnt(0)
	v_pk_mul_f32 v[4:5], s[0:1], v[4:5]
	s_waitcnt vmcnt(0)
	v_pk_mul_f32 v[2:3], s[0:1], v[2:3]
	s_lshl_b64 s[0:1], s[2:3], 2
	s_add_u32 s0, s8, s0
	v_sub_f32_e32 v1, v4, v5
	s_addc_u32 s1, s9, s1
	global_store_dword v0, v1, s[0:1] sc1
	v_sub_f32_e32 v2, v2, v3
	global_store_dword v0, v2, s[0:1] offset:256 sc1
	s_endpgm

	.amdhsa_kernel _Z7k_spmm1PKiS0_PKfPK15HIP_vector_typeIjLj2EES0_S2_S2_Pfff
		.amdhsa_group_segment_fixed_size 0
		.amdhsa_private_segment_fixed_size 0
		.amdhsa_kernarg_size 72
		.amdhsa_user_sgpr_count 2
		.amdhsa_user_sgpr_dispatch_ptr 0
		.amdhsa_user_sgpr_queue_ptr 0
		.amdhsa_user_sgpr_kernarg_segment_ptr 1
		.amdhsa_user_sgpr_dispatch_id 0
		.amdhsa_user_sgpr_kernarg_preload_length 0
		.amdhsa_user_sgpr_kernarg_preload_offset 0
		.amdhsa_user_sgpr_private_segment_size 0
		.amdhsa_uses_dynamic_stack 0
		.amdhsa_enable_private_segment 0
		.amdhsa_system_sgpr_workgroup_id_x 1
		.amdhsa_system_sgpr_workgroup_id_y 0
		.amdhsa_system_sgpr_workgroup_id_z 0
		.amdhsa_system_sgpr_workgroup_info 0
		.amdhsa_system_vgpr_workitem_id 0
		.amdhsa_next_free_vgpr 41
		.amdhsa_next_free_sgpr 32
		.amdhsa_accum_offset 44
		.amdhsa_reserve_vcc 0
		.amdhsa_float_round_mode_32 0
		.amdhsa_float_round_mode_16_64 0
		.amdhsa_float_denorm_mode_32 3
		.amdhsa_float_denorm_mode_16_64 3
		.amdhsa_dx10_clamp 1
		.amdhsa_ieee_mode 1
		.amdhsa_fp16_overflow 0
		.amdhsa_tg_split 0
		.amdhsa_exception_fp_ieee_invalid_op 0
		.amdhsa_exception_fp_denorm_src 0
		.amdhsa_exception_fp_ieee_div_zero 0
		.amdhsa_exception_fp_ieee_overflow 0
		.amdhsa_exception_fp_ieee_underflow 0
		.amdhsa_exception_fp_ieee_inexact 0
		.amdhsa_exception_int_div_zero 0
	.end_amdhsa_kernel

amdhsa.kernels:
  - .agpr_count:     0
    .args:
      - .actual_access:  read_only
        .address_space:  global
        .offset:         0
        .size:           8
        .value_kind:     global_buffer
      - .actual_access:  read_only
        .address_space:  global
        .offset:         8
        .size:           8
        .value_kind:     global_buffer
      - .actual_access:  write_only
        .address_space:  global
        .offset:         16
        .size:           8
        .value_kind:     global_buffer
      - .actual_access:  write_only
        .address_space:  global
        .offset:         24
        .size:           8
        .value_kind:     global_buffer
      - .actual_access:  write_only
        .address_space:  global
        .offset:         32
        .size:           8
        .value_kind:     global_buffer
      - .actual_access:  read_only
        .address_space:  global
        .offset:         40
        .size:           8
        .value_kind:     global_buffer
    .group_segment_fixed_size: 1024
    .kernarg_segment_align: 8
    .kernarg_segment_size: 48
    .language:       OpenCL C
    .language_version:
      - 2
      - 0
    .max_flat_workgroup_size: 1024
    .name:           _Z7k_sort2PKiPKfPiS3_S3_Pf
    .private_segment_fixed_size: 0
    .sgpr_count:     18
    .sgpr_spill_count: 0
    .symbol:         _Z7k_sort2PKiPKfPiS3_S3_Pf.kd
    .uniform_work_group_size: 1
    .uses_dynamic_stack: false
    .vgpr_count:     25
    .vgpr_spill_count: 0
    .wavefront_size: 64
  - .agpr_count:     0
    .args:
      - .actual_access:  read_only
        .address_space:  global
        .offset:         0
        .size:           8
        .value_kind:     global_buffer
      - .actual_access:  read_only
        .address_space:  global
        .offset:         8
        .size:           8
        .value_kind:     global_buffer
      - .actual_access:  read_only
        .address_space:  global
        .offset:         16
        .size:           8
        .value_kind:     global_buffer
      - .actual_access:  read_only
        .address_space:  global
        .offset:         24
        .size:           8
        .value_kind:     global_buffer
      - .actual_access:  read_only
        .address_space:  global
        .offset:         32
        .size:           8
        .value_kind:     global_buffer
      - .actual_access:  read_only
        .address_space:  global
        .offset:         40
        .size:           8
        .value_kind:     global_buffer
      - .address_space:  global
        .offset:         48
        .size:           8
        .value_kind:     global_buffer
      - .address_space:  global
        .offset:         56
        .size:           8
        .value_kind:     global_buffer
      - .offset:         64
        .size:           4
        .value_kind:     by_value
      - .offset:         68
        .size:           4
        .value_kind:     by_value
    .group_segment_fixed_size: 0
    .kernarg_segment_align: 8
    .kernarg_segment_size: 72
    .language:       OpenCL C
    .language_version:
      - 2
      - 0
    .max_flat_workgroup_size: 512
    .name:           _Z7k_spmm1PKiS0_PKfPK15HIP_vector_typeIjLj2EES0_S2_S2_Pfff
    .private_segment_fixed_size: 0
    .sgpr_count:     38
    .sgpr_spill_count: 0
    .symbol:         _Z7k_spmm1PKiS0_PKfPK15HIP_vector_typeIjLj2EES0_S2_S2_Pfff.kd
    .uniform_work_group_size: 1
    .uses_dynamic_stack: false
    .vgpr_count:     41
    .vgpr_spill_count: 0
    .wavefront_size: 64
  - .agpr_count:     0
    .args:
      - .address_space:  global
        .offset:         0
        .size:           8
        .value_kind:     global_buffer
      - .actual_access:  read_only
        .address_space:  global
        .offset:         8
        .size:           8
        .value_kind:     global_buffer
      - .actual_access:  read_only
        .address_space:  global
        .offset:         16
        .size:           8
        .value_kind:     global_buffer
      - .actual_access:  write_only
        .address_space:  global
        .offset:         24
        .size:           8
        .value_kind:     global_buffer
    .group_segment_fixed_size: 32768
    .kernarg_segment_align: 8
    .kernarg_segment_size: 32
    .language:       OpenCL C
    .language_version:
      - 2
      - 0
    .max_flat_workgroup_size: 512
    .name:           _Z7k_conv1PKfS0_S0_Pf
    .private_segment_fixed_size: 0
    .sgpr_count:     46
    .sgpr_spill_count: 0
    .symbol:         _Z7k_conv1PKfS0_S0_Pf.kd
    .uniform_work_group_size: 1
    .uses_dynamic_stack: false
    .vgpr_count:     107
    .vgpr_spill_count: 0
    .wavefront_size: 64
  - .agpr_count:     0
    .args:
      - .actual_access:  read_only
        .address_space:  global
        .offset:         0
        .size:           8
        .value_kind:     global_buffer
      - .actual_access:  read_only
        .address_space:  global
        .offset:         8
        .size:           8
        .value_kind:     global_buffer
      - .actual_access:  read_only
        .address_space:  global
        .offset:         16
        .size:           8
        .value_kind:     global_buffer
      - .address_space:  global
        .offset:         24
        .size:           8
        .value_kind:     global_buffer
      - .actual_access:  read_only
        .address_space:  global
        .offset:         32
        .size:           8
        .value_kind:     global_buffer
      - .actual_access:  read_only
        .address_space:  global
        .offset:         40
        .size:           8
        .value_kind:     global_buffer
      - .actual_access:  write_only
        .address_space:  global
        .offset:         48
        .size:           8
        .value_kind:     global_buffer
      - .actual_access:  write_only
        .address_space:  global
        .offset:         56
        .size:           8
        .value_kind:     global_buffer
      - .actual_access:  write_only
        .address_space:  global
        .offset:         64
        .size:           8
        .value_kind:     global_buffer
    .group_segment_fixed_size: 139392
    .kernarg_segment_align: 8
    .kernarg_segment_size: 72
    .language:       OpenCL C
    .language_version:
      - 2
      - 0
    .max_flat_workgroup_size: 512
    .name:           _Z6k_rec2PKiS0_S0_PK15HIP_vector_typeIjLj4EEPKfS6_PS2_PS1_IjLj2EEPf
    .private_segment_fixed_size: 0
    .sgpr_count:     75
    .sgpr_spill_count: 0
    .symbol:         _Z6k_rec2PKiS0_S0_PK15HIP_vector_typeIjLj4EEPKfS6_PS2_PS1_IjLj2EEPf.kd
    .uniform_work_group_size: 1
    .uses_dynamic_stack: false
    .vgpr_count:     254
    .vgpr_spill_count: 0
    .wavefront_size: 64
  - .agpr_count:     0
    .args:
      - .address_space:  global
        .offset:         0
        .size:           8
        .value_kind:     global_buffer
      - .address_space:  global
        .offset:         8
        .size:           8
        .value_kind:     global_buffer
      - .actual_access:  read_only
        .address_space:  global
        .offset:         16
        .size:           8
        .value_kind:     global_buffer
      - .actual_access:  read_only
        .address_space:  global
        .offset:         24
        .size:           8
        .value_kind:     global_buffer
      - .actual_access:  read_only
        .address_space:  global
        .offset:         32
        .size:           8
        .value_kind:     global_buffer
      - .actual_access:  read_only
        .address_space:  global
        .offset:         40
        .size:           8
        .value_kind:     global_buffer
      - .actual_access:  write_only
        .address_space:  global
        .offset:         48
        .size:           8
        .value_kind:     global_buffer
      - .actual_access:  write_only
        .address_space:  global
        .offset:         56
        .size:           8
        .value_kind:     global_buffer
    .group_segment_fixed_size: 127376
    .kernarg_segment_align: 8
    .kernarg_segment_size: 64
    .language:       OpenCL C
    .language_version:
      - 2
      - 0
    .max_flat_workgroup_size: 1024
    .name:           _Z7k_gemm2PK15HIP_vector_typeIjLj4EEPKS_IjLj2EEPKfS2_S2_S7_PtS8_
    .private_segment_fixed_size: 0
    .sgpr_count:     26
    .sgpr_spill_count: 0
    .symbol:         _Z7k_gemm2PK15HIP_vector_typeIjLj4EEPKS_IjLj2EEPKfS2_S2_S7_PtS8_.kd
    .uniform_work_group_size: 1
    .uses_dynamic_stack: false
    .vgpr_count:     115
    .vgpr_spill_count: 0
    .wavefront_size: 64
  - .agpr_count:     32
    .args:
      - .address_space:  global
        .offset:         0
        .size:           8
        .value_kind:     global_buffer
      - .address_space:  global
        .offset:         8
        .size:           8
        .value_kind:     global_buffer
      - .address_space:  global
        .offset:         16
        .size:           8
        .value_kind:     global_buffer
      - .actual_access:  write_only
        .address_space:  global
        .offset:         24
        .size:           8
        .value_kind:     global_buffer
    .group_segment_fixed_size: 65536
    .kernarg_segment_align: 8
    .kernarg_segment_size: 32
    .language:       OpenCL C
    .language_version:
      - 2
      - 0
    .max_flat_workgroup_size: 256
    .name:           _Z5k_fc1PKtS0_PKfPf
    .private_segment_fixed_size: 0
    .sgpr_count:     49
    .sgpr_spill_count: 0
    .symbol:         _Z5k_fc1PKtS0_PKfPf.kd
    .uniform_work_group_size: 1
    .uses_dynamic_stack: false
    .vgpr_count:     172
    .vgpr_spill_count: 0
    .wavefront_size: 64
  - .agpr_count:     0
    .args:
      - .actual_access:  read_only
        .address_space:  global
        .offset:         0
        .size:           8
        .value_kind:     global_buffer
      - .actual_access:  read_only
        .address_space:  global
        .offset:         8
        .size:           8
        .value_kind:     global_buffer
      - .actual_access:  read_only
        .address_space:  global
        .offset:         16
        .size:           8
        .value_kind:     global_buffer
      - .actual_access:  read_only
        .address_space:  global
        .offset:         24
        .size:           8
        .value_kind:     global_buffer
      - .actual_access:  write_only
        .address_space:  global
        .offset:         32
        .size:           8
        .value_kind:     global_buffer
    .group_segment_fixed_size: 2048
    .kernarg_segment_align: 8
    .kernarg_segment_size: 40
    .language:       OpenCL C
    .language_version:
      - 2
      - 0
    .max_flat_workgroup_size: 512
    .name:           _Z5k_fc2PKfS0_S0_S0_Pf
    .private_segment_fixed_size: 0
    .sgpr_count:     18
    .sgpr_spill_count: 0
    .symbol:         _Z5k_fc2PKfS0_S0_S0_Pf.kd
    .uniform_work_group_size: 1
    .uses_dynamic_stack: false
    .vgpr_count:     96
    .vgpr_spill_count: 0
    .wavefront_size: 64
  - .agpr_count:     0
    .args:
      - .actual_access:  read_only
        .address_space:  global
        .offset:         0
        .size:           8
        .value_kind:     global_buffer
      - .actual_access:  read_only
        .address_space:  global
        .offset:         8
        .size:           8
        .value_kind:     global_buffer
      - .actual_access:  read_only
        .address_space:  global
        .offset:         16
        .size:           8
        .value_kind:     global_buffer
      - .actual_access:  read_only
        .address_space:  global
        .offset:         24
        .size:           8
        .value_kind:     global_buffer
      - .actual_access:  write_only
        .address_space:  global
        .offset:         32
        .size:           8
        .value_kind:     global_buffer
      - .actual_access:  write_only
        .address_space:  global
        .offset:         40
        .size:           8
        .value_kind:     global_buffer
      - .actual_access:  write_only
        .address_space:  global
        .offset:         48
        .size:           8
        .value_kind:     global_buffer
      - .actual_access:  write_only
        .address_space:  global
        .offset:         56
        .size:           8
        .value_kind:     global_buffer
      - .actual_access:  write_only
        .address_space:  global
        .offset:         64
        .size:           8
        .value_kind:     global_buffer
    .group_segment_fixed_size: 16640
    .kernarg_segment_align: 8
    .kernarg_segment_size: 72
    .language:       OpenCL C
    .language_version:
      - 2
      - 0
    .max_flat_workgroup_size: 256
    .name:           _Z7k_prepAPKiS0_PKfS2_PiS3_PtS4_Pf
    .private_segment_fixed_size: 0
    .sgpr_count:     20
    .sgpr_spill_count: 0
    .symbol:         _Z7k_prepAPKiS0_PKfS2_PiS3_PtS4_Pf.kd
    .uniform_work_group_size: 1
    .uses_dynamic_stack: false
    .vgpr_count:     24
    .vgpr_spill_count: 0
    .wavefront_size: 64
  - .agpr_count:     0
    .args:
      - .actual_access:  read_only
        .address_space:  global
        .offset:         0
        .size:           8
        .value_kind:     global_buffer
      - .actual_access:  read_only
        .address_space:  global
        .offset:         8
        .size:           8
        .value_kind:     global_buffer
      - .actual_access:  read_only
        .address_space:  global
        .offset:         16
        .size:           8
        .value_kind:     global_buffer
      - .actual_access:  write_only
        .address_space:  global
        .offset:         24
        .size:           8
        .value_kind:     global_buffer
      - .actual_access:  write_only
        .address_space:  global
        .offset:         32
        .size:           8
        .value_kind:     global_buffer
      - .actual_access:  read_only
        .address_space:  global
        .offset:         40
        .size:           8
        .value_kind:     global_buffer
      - .actual_access:  read_only
        .address_space:  global
        .offset:         48
        .size:           8
        .value_kind:     global_buffer
      - .actual_access:  read_only
        .address_space:  global
        .offset:         56
        .size:           8
        .value_kind:     global_buffer
      - .actual_access:  read_only
        .address_space:  global
        .offset:         64
        .size:           8
        .value_kind:     global_buffer
      - .actual_access:  read_only
        .address_space:  global
        .offset:         72
        .size:           8
        .value_kind:     global_buffer
      - .actual_access:  read_only
        .address_space:  global
        .offset:         80
        .size:           8
        .value_kind:     global_buffer
      - .actual_access:  read_only
        .address_space:  global
        .offset:         88
        .size:           8
        .value_kind:     global_buffer
      - .actual_access:  write_only
        .address_space:  global
        .offset:         96
        .size:           8
        .value_kind:     global_buffer
    .group_segment_fixed_size: 0
    .kernarg_segment_align: 8
    .kernarg_segment_size: 104
    .language:       OpenCL C
    .language_version:
      - 2
      - 0
    .max_flat_workgroup_size: 256
    .name:           _Z7k_prepBPKiS0_PKfP15HIP_vector_typeIjLj2EEPiS0_S0_S2_S0_S0_S0_S2_Pj
    .private_segment_fixed_size: 0
    .sgpr_count:     21
    .sgpr_spill_count: 0
    .symbol:         _Z7k_prepBPKiS0_PKfP15HIP_vector_typeIjLj2EEPiS0_S0_S2_S0_S0_S0_S2_Pj.kd
    .uniform_work_group_size: 1
    .uses_dynamic_stack: false
    .vgpr_count:     14
    .vgpr_spill_count: 0
    .wavefront_size: 64
